# attention: waves 4-7 take the tile barrier before their softmax scaling section and issue DMA at tile top (phase shift between the two waves of a SIMD)
# baseline (speedup 1.0000x reference)
.LBB0_1343:
	s_and_b32 s3, s21, 3
	s_and_b64 s[4:5], exec, s[34:35]
	s_cselect_b32 s3, -1, s3
	s_cmp_eq_u32 s3, 2
	s_movk_i32 s4, 0x3080
	s_cselect_b32 s4, 0x2000, s4
	s_cmp_lg_u32 s3, 1
	s_cselect_b32 s4, s4, 0x1000
	s_cmp_gt_i32 s3, 0
	s_cselect_b32 s8, s4, 0
	s_mul_i32 s18, s8, 0xe00
	v_readlane_b32 s4, v253, 7
	v_readlane_b32 s5, v253, 8
	s_add_u32 s4, s4, s18
	v_lshlrev_b32_e32 v2, 8, v181
	v_mov_b32_e32 v3, v99
	v_lshl_add_u32 v7, v7, 7, v14
	s_addc_u32 s5, s5, 0
	v_lshlrev_b64 v[50:51], 1, v[2:3]
	v_cvt_pk_bf16_f32 v5, v5, v99
	ds_write_b16 v7, v5
	v_cvt_pk_bf16_f32 v4, v4, v99
	v_lshl_add_u64 v[2:3], s[4:5], 0, v[50:51]
	ds_write_b16 v7, v4 offset:32
	v_ashrrev_i32_e32 v4, 4, v6
	v_lshlrev_b32_e32 v5, 3, v6
	s_movk_i32 s4, 0x700
	v_and_b32_e32 v7, 0x78, v5
	v_mul_lo_u32 v8, v4, s4
	v_or_b32_e32 v8, v8, v7
	v_lshlrev_b32_e32 v52, 1, v8
	v_readfirstlane_b32 s4, v2
	v_readfirstlane_b32 s5, v3
	s_waitcnt lgkmcnt(0)
	s_barrier
	v_add_u32_e32 v54, 0x1c000, v52
	s_nop 1
	global_load_dwordx4 v[8:11], v52, s[4:5] offset:1792
	global_load_dwordx4 v[14:17], v54, s[4:5] offset:1792
	s_lshl_b32 s22, s8, 7
	v_readlane_b32 s8, v253, 5
	v_lshlrev_b32_e32 v26, 4, v6
	v_readlane_b32 s9, v253, 6
	s_add_u32 s24, s8, s22
	v_ashrrev_i32_e32 v13, 3, v6
	v_and_b32_e32 v30, 0x70, v26
	s_addc_u32 s25, s9, 0
	v_lshl_or_b32 v56, v13, 7, v30
	global_load_dwordx4 v[18:21], v52, s[4:5] offset:1536
	global_load_dwordx4 v[22:25], v54, s[4:5] offset:1536
	global_load_dwordx4 v[26:29], v56, s[24:25]
	v_lshlrev_b32_e32 v31, 7, v194
	v_lshlrev_b32_e32 v12, 1, v12
	v_readlane_b32 s4, v255, 34
	v_lshlrev_b32_e32 v32, 1, v4
	v_lshrrev_b32_e32 v33, 1, v4
	v_add3_u32 v12, s4, v31, v12
	v_and_b32_e32 v31, 0xfffff0, v4
	v_and_b32_e32 v35, 3, v4
	v_add_u32_e32 v36, 32, v4
	s_add_i32 s4, 0, 0x14000
	ds_read_b128 v[144:147], v12
	ds_read_b128 v[140:143], v12 offset:32
	ds_read_b128 v[136:139], v12 offset:64
	ds_read_b128 v[132:135], v12 offset:96
	v_and_or_b32 v12, v32, 8, v31
	v_and_or_b32 v31, v33, 4, v35
	v_and_b32_e32 v32, 0xfffff0, v36
	v_lshlrev_b32_e32 v33, 1, v36
	s_and_b64 s[0:1], s[0:1], exec
	v_bfe_u32 v34, v5, 5, 2
	v_lshrrev_b32_e32 v12, 1, v12
	v_and_or_b32 v32, v33, 8, v32
	s_cselect_b32 s5, 0x104, 4
	s_cmp_lt_u32 s3, 2
	v_lshlrev_b32_e32 v7, 1, v7
	v_or_b32_e32 v12, v12, v34
	v_lshrrev_b32_e32 v32, 1, v32
	s_cselect_b32 s3, 64, 0x42
	s_and_b64 s[0:1], exec, s[34:35]
	v_lshlrev_b32_e32 v31, 6, v31
	v_and_b32_e32 v35, 48, v7
	v_lshlrev_b32_e32 v12, 9, v12
	v_or_b32_e32 v32, v32, v34
	s_cselect_b32 s3, s5, s3
	s_add_i32 s0, 0, 0x8000
	v_lshlrev_b32_e32 v32, 9, v32
	v_or3_b32 v12, v12, v31, v35
	s_cmp_lg_u32 s0, -1
	v_or3_b32 v31, v32, v31, v35
	v_add_u32_e32 v205, 0, v12
	s_cselect_b32 s0, s0, 0
	s_movk_i32 s8, 0x70
	v_add_u32_e32 v206, 0, v31
	s_waitcnt vmcnt(0)
	v_mov_b32_e32 v12, s0
	s_movk_i32 s0, 0x180
	v_mul_lo_u32 v4, v4, s0
	v_bitop3_b32 v37, v98, v5, s8 bitop3:0x78
	s_waitcnt vmcnt(4)
	ds_write_b128 v205, v[8:11]
	s_waitcnt vmcnt(3)
	ds_write_b128 v206, v[14:17]
	v_lshrrev_b32_e32 v8, 1, v6
	v_bitop3_b32 v7, v7, v8, s8 bitop3:0x78
	v_add3_u32 v207, v7, v4, 0
	v_mul_lo_u32 v4, v13, s0
	v_or_b32_e32 v7, 0x100, v30
	v_and_b32_e32 v8, 0x70, v6
	v_mad_u32_u24 v53, v195, s0, v12
	v_xad_u32 v4, v7, v8, v4
	v_add_u32_e32 v201, v37, v53
	v_add_u32_e32 v208, 0, v4
	s_waitcnt vmcnt(2)
	ds_write_b128 v207, v[18:21] offset:32768
	s_waitcnt vmcnt(1)
	ds_write_b128 v207, v[22:25] offset:45056
	s_waitcnt vmcnt(0)
	ds_write_b128 v208, v[26:29] offset:32768
	s_waitcnt lgkmcnt(0)
	s_barrier
	ds_read_b128 v[8:11], v201
	ds_read_b128 v[12:15], v201 offset:128
	s_waitcnt lgkmcnt(1)
	v_mfma_f32_32x32x16_bf16 v[18:33], v[8:11], v[128:131], 0
	ds_read_b128 v[8:11], v201 offset:12288
	ds_read_b128 v[60:63], v201 offset:256
	v_and_b32_e32 v4, 0x70, v5
	v_bitop3_b32 v5, v98, v4, 32 bitop3:0x36
	v_add_u32_e32 v203, v5, v53
	v_bitop3_b32 v5, v98, v4, 64 bitop3:0x36
	v_add_u32_e32 v204, v5, v53
	s_waitcnt lgkmcnt(1)
	v_mfma_f32_32x32x16_bf16 v[34:49], v[8:11], v[128:131], 0
	ds_read_b128 v[8:11], v203
	ds_read_b128 v[64:67], v203 offset:128
	ds_read_b128 v[68:71], v203 offset:256
	s_movk_i32 s0, 0x60
	v_bitop3_b32 v4, v98, v4, s0 bitop3:0x36
	v_add_u32_e32 v202, v4, v53
	s_mov_b64 s[0:1], 0x38700
	v_lshl_add_u64 v[4:5], v[2:3], 0, s[0:1]
	s_waitcnt lgkmcnt(2)
	v_mfma_f32_32x32x16_bf16 v[18:33], v[8:11], v[124:127], v[18:33]
	ds_read_b128 v[8:11], v203 offset:12288
	s_mov_b64 s[0:1], 0x38600
	v_lshl_add_u64 v[2:3], v[2:3], 0, s[0:1]
	v_readfirstlane_b32 s0, v4
	v_readfirstlane_b32 s1, v5
	v_readfirstlane_b32 s8, v2
	v_readfirstlane_b32 s9, v3
	s_waitcnt lgkmcnt(0)
	v_mfma_f32_32x32x16_bf16 v[34:49], v[8:11], v[124:127], v[34:49]
	ds_read_b128 v[8:11], v204
	ds_read_b128 v[72:75], v204 offset:128
	ds_read_b128 v[76:79], v204 offset:256
	v_mov_b32_e32 v57, v99
	v_add_u32_e32 v209, 0x3000, v207
	s_cmp_lg_u32 0, -1
	v_lshlrev_b32_e32 v4, 1, v58
	v_and_b32_e32 v4, 32, v4
	s_waitcnt lgkmcnt(2)
	v_mfma_f32_32x32x16_bf16 v[18:33], v[8:11], v[120:123], v[18:33]
	ds_read_b128 v[8:11], v204 offset:12288
	s_mov_b32 s36, s63
	s_mov_b32 s37, s63
	s_mov_b32 s19, s63
	s_mov_b32 s38, s63
	s_mov_b32 s39, s63
	s_mov_b32 s40, s63
	s_waitcnt lgkmcnt(0)
	v_mfma_f32_32x32x16_bf16 v[34:49], v[8:11], v[120:123], v[34:49]
	ds_read_b128 v[8:11], v202
	ds_read_b128 v[80:83], v202 offset:128
	s_mov_b32 s41, s63
	s_mov_b32 s42, s63
	s_mov_b32 s43, s63
	s_mov_b32 s44, s63
	s_mov_b32 s45, s63
	s_mov_b32 s46, s63
	s_waitcnt lgkmcnt(1)
	v_mfma_f32_32x32x16_bf16 v[18:33], v[8:11], v[116:119], v[18:33]
	ds_read_b128 v[8:11], v202 offset:12288
	ds_read_b128 v[84:87], v202 offset:256
	s_mov_b32 s47, s63
	s_mov_b32 s48, s63
	s_mov_b32 s49, s63
	s_mov_b32 s50, s63
	s_mov_b32 s51, s63
	s_mov_b32 s23, s63
	v_mfma_f32_32x32x16_bf16 v[18:33], v[12:15], v[112:115], v[18:33]
	v_mov_b32_e32 v53, v99
	v_mov_b32_e32 v55, v99
	v_lshl_add_u64 v[182:183], s[22:23], 0, v[56:57]
	v_mov_b32_e32 v227, 0x3200
	v_mov_b32_e32 v199, 0
	s_waitcnt lgkmcnt(1)
	v_mfma_f32_32x32x16_bf16 v[34:49], v[8:11], v[116:119], v[34:49]
	ds_read_b128 v[8:11], v201 offset:12416
	ds_read_b128 v[12:15], v201 offset:12544
	v_mfma_f32_32x32x16_bf16 v[18:33], v[64:67], v[108:111], v[18:33]
	s_waitcnt lgkmcnt(1)
	v_mfma_f32_32x32x16_bf16 v[34:49], v[8:11], v[112:115], v[34:49]
	ds_read_b128 v[8:11], v203 offset:12416
	ds_read_b128 v[64:67], v203 offset:12544
	v_mfma_f32_32x32x16_bf16 v[18:33], v[72:75], v[104:107], v[18:33]
	s_waitcnt lgkmcnt(1)
	v_mfma_f32_32x32x16_bf16 v[34:49], v[8:11], v[108:111], v[34:49]
	ds_read_b128 v[8:11], v204 offset:12416
	ds_read_b128 v[72:75], v204 offset:12544
	v_mfma_f32_32x32x16_bf16 v[18:33], v[80:83], v[100:103], v[18:33]
	s_waitcnt lgkmcnt(1)
	v_mfma_f32_32x32x16_bf16 v[34:49], v[8:11], v[104:107], v[34:49]
	ds_read_b128 v[8:11], v202 offset:12416
	ds_read_b128 v[80:83], v202 offset:12544
	v_mfma_f32_32x32x16_bf16 v[18:33], v[60:63], v[144:147], v[18:33]
	global_load_dwordx4 v[60:63], v54, s[0:1]
	global_load_dwordx4 v[88:91], v52, s[8:9]
	global_load_dwordx4 v[92:95], v52, s[0:1]
	global_load_dwordx4 v[148:151], v54, s[8:9]
	s_movk_i32 s0, 0x2000
	s_mov_b32 s8, 2
	s_waitcnt lgkmcnt(1)
	v_mfma_f32_32x32x16_bf16 v[34:49], v[8:11], v[100:103], v[34:49]
	v_lshl_add_u64 v[8:9], s[24:25], 0, v[56:57]
	v_add_co_u32_e32 v2, vcc, s0, v8
	v_cmp_gt_u32_e64 s[0:1], 32, v58
	s_nop 0
	v_addc_co_u32_e32 v3, vcc, 0, v9, vcc
	global_load_dwordx4 v[152:155], v[2:3], off
	v_mfma_f32_32x32x16_bf16 v[18:33], v[68:71], v[140:143], v[18:33]
	s_waitcnt vmcnt(0)
	s_waitcnt vmcnt(2)
	ds_write_b128 v205, v[92:95] offset:16384
	ds_write_b128 v206, v[60:63] offset:16384
	ds_write_b128 v207, v[88:91] offset:57344
	s_waitcnt vmcnt(1)
	ds_write_b128 v209, v[148:151] offset:57344
	s_waitcnt vmcnt(0)
	ds_write_b128 v208, v[152:155] offset:57344
	v_mfma_f32_32x32x16_bf16 v[34:49], v[12:15], v[144:147], v[34:49]
	v_and_b32_e32 v2, 0x3fffffc0, v6
	v_lshl_add_u32 v196, v2, 2, s4
	s_cselect_b32 s4, 0, 0
	v_lshlrev_b32_e32 v3, 4, v58
	v_lshlrev_b32_e32 v2, 3, v58
	v_and_b32_e32 v3, 0xc0, v3
	v_and_or_b32 v3, v2, 24, v3
	v_mfma_f32_32x32x16_bf16 v[18:33], v[76:79], v[136:139], v[18:33]
	v_and_b32_e32 v2, 0x100, v2
	v_or3_b32 v59, v3, v4, v2
	v_mov_b64_e32 v[2:3], s[36:37]
	v_add_u32_e32 v200, s4, v59
	v_mov_b64_e32 v[16:17], s[50:51]
	v_mov_b64_e32 v[4:5], s[38:39]
	v_mov_b64_e32 v[6:7], s[40:41]
	v_mfma_f32_32x32x16_bf16 v[34:49], v[64:67], v[140:143], v[34:49]
	v_mov_b64_e32 v[8:9], s[42:43]
	v_mov_b64_e32 v[10:11], s[44:45]
	v_mov_b64_e32 v[12:13], s[46:47]
	v_mov_b64_e32 v[14:15], s[48:49]
	v_lshl_add_u32 v197, v195, 2, v196
	s_waitcnt lgkmcnt(0)
	s_barrier
	v_mfma_f32_32x32x16_bf16 v[18:33], v[84:87], v[132:135], v[18:33]
	v_mfma_f32_32x32x16_bf16 v[34:49], v[72:75], v[136:139], v[34:49]
	s_nop 10
	v_max_f32_e32 v64, v19, v19
	v_max_f32_e32 v65, v18, v18
	v_max_f32_e32 v64, v65, v64
	v_max3_f32 v64, v64, v20, v21
	v_max3_f32 v64, v64, v22, v23
	v_max3_f32 v64, v64, v24, v25
	v_max3_f32 v64, v64, v26, v27
	v_mfma_f32_32x32x16_bf16 v[34:49], v[80:83], v[132:135], v[34:49]
	v_max3_f32 v64, v64, v28, v29
	v_max3_f32 v64, v64, v30, v31
	v_max3_f32 v64, v64, v32, v33
	s_nop 8
	v_max3_f32 v64, v64, v34, v35
	v_max3_f32 v64, v64, v36, v37
	v_max3_f32 v64, v64, v38, v39
	v_max3_f32 v64, v64, v40, v41
	v_max3_f32 v64, v64, v42, v43
	v_max3_f32 v64, v64, v44, v45
	v_max3_f32 v64, v64, v46, v47
	v_max3_f32 v64, v64, v48, v49
	v_mov_b32_e32 v65, v64
	s_nop 1
	v_permlane32_swap_b32_e32 v64, v65
	v_max_f32_e32 v65, v65, v65
	v_max_f32_e32 v64, v64, v64
	v_max_f32_e32 v64, v64, v65
	v_max_f32_e32 v60, 0xf149f2ca, v64
	v_sub_f32_e32 v61, 0xf149f2ca, v60
	v_mul_f32_e32 v61, 0x3dd53b94, v61
	v_add_f32_e32 v65, 0x7149f2ca, v64
	v_exp_f32_e32 v61, v61
	v_cmp_ge_f32_e32 vcc, s11, v65
	s_cmp_eq_u64 vcc, exec
	s_cselect_b64 vcc, -1, 0
	v_cndmask_b32_e64 v210, v61, 1.0, vcc
	v_mov_b32_e32 v61, 0xf149f2ca
	v_cndmask_b32_e32 v211, v60, v61, vcc
	v_mul_f32_e32 v60, 0xbdd53b94, v211
	v_fmamk_f32 v18, v18, 0x3dd53b94, v60
	v_exp_f32_e32 v169, v18
	v_fmamk_f32 v18, v19, 0x3dd53b94, v60
	v_exp_f32_e32 v191, v18
	v_fmamk_f32 v18, v20, 0x3dd53b94, v60
	v_exp_f32_e32 v170, v18
	v_fmamk_f32 v18, v21, 0x3dd53b94, v60
	v_exp_f32_e32 v192, v18
	v_fmamk_f32 v18, v22, 0x3dd53b94, v60
	v_exp_f32_e32 v190, v18
	v_fmamk_f32 v18, v23, 0x3dd53b94, v60
	v_exp_f32_e32 v193, v18
	v_fmamk_f32 v18, v24, 0x3dd53b94, v60
	v_exp_f32_e32 v171, v18
	v_fmamk_f32 v18, v25, 0x3dd53b94, v60
	v_exp_f32_e32 v189, v18
	v_fmamk_f32 v18, v26, 0x3dd53b94, v60
	v_exp_f32_e32 v173, v18
	v_fmamk_f32 v18, v27, 0x3dd53b94, v60
	v_exp_f32_e32 v175, v18
	v_fmamk_f32 v18, v28, 0x3dd53b94, v60
	v_exp_f32_e32 v174, v18
	v_fmamk_f32 v18, v29, 0x3dd53b94, v60
	v_exp_f32_e32 v188, v18
	v_fmamk_f32 v18, v30, 0x3dd53b94, v60
	v_exp_f32_e32 v164, v18
	v_fmamk_f32 v18, v31, 0x3dd53b94, v60
	v_pk_fma_f32 v[148:149], v[48:49], s[56:57], v[60:61] op_sel_hi:[1,0,0]
	v_pk_fma_f32 v[154:155], v[46:47], s[56:57], v[60:61] op_sel_hi:[1,0,0]
	v_pk_fma_f32 v[158:159], v[44:45], s[56:57], v[60:61] op_sel_hi:[1,0,0]
	v_pk_fma_f32 v[150:151], v[42:43], s[56:57], v[60:61] op_sel_hi:[1,0,0]
	v_pk_fma_f32 v[152:153], v[40:41], s[56:57], v[60:61] op_sel_hi:[1,0,0]
	v_pk_fma_f32 v[156:157], v[38:39], s[56:57], v[60:61] op_sel_hi:[1,0,0]
	v_pk_fma_f32 v[160:161], v[36:37], s[56:57], v[60:61] op_sel_hi:[1,0,0]
	v_pk_fma_f32 v[162:163], v[34:35], s[56:57], v[60:61] op_sel_hi:[1,0,0]
	v_exp_f32_e32 v166, v18
	v_fmamk_f32 v18, v32, 0x3dd53b94, v60
	v_fmac_f32_e32 v60, 0x3dd53b94, v33
	v_exp_f32_e32 v165, v18
	v_exp_f32_e32 v167, v60
	s_addk_i32 s4, 0x4000
	v_lshl_add_u64 v[18:19], s[18:19], 0, v[50:51]
	v_add_u32_e32 v198, s4, v59
	v_lshl_add_u64 v[184:185], v[18:19], 0, v[54:55]
	v_lshl_add_u64 v[186:187], v[18:19], 0, v[52:53]
	v_mov_b64_e32 v[64:65], v[16:17]
	v_mov_b64_e32 v[48:49], v[16:17]
	v_mov_b64_e32 v[32:33], v[16:17]
	v_mov_b64_e32 v[62:63], v[14:15]
	v_mov_b64_e32 v[60:61], v[12:13]
	v_mov_b64_e32 v[58:59], v[10:11]
	v_mov_b64_e32 v[56:57], v[8:9]
	v_mov_b64_e32 v[54:55], v[6:7]
	v_mov_b64_e32 v[52:53], v[4:5]
	v_mov_b64_e32 v[50:51], v[2:3]
	v_mov_b64_e32 v[46:47], v[14:15]
	v_mov_b64_e32 v[44:45], v[12:13]
	v_mov_b64_e32 v[42:43], v[10:11]
	v_mov_b64_e32 v[40:41], v[8:9]
	v_mov_b64_e32 v[38:39], v[6:7]
	v_mov_b64_e32 v[36:37], v[4:5]
	v_mov_b64_e32 v[34:35], v[2:3]
	v_mov_b64_e32 v[30:31], v[14:15]
	v_mov_b64_e32 v[28:29], v[12:13]
	v_mov_b64_e32 v[26:27], v[10:11]
	v_mov_b64_e32 v[24:25], v[8:9]
	v_mov_b64_e32 v[22:23], v[6:7]
	v_mov_b64_e32 v[20:21], v[4:5]
	v_mov_b64_e32 v[18:19], v[2:3]
	v_and_b32_e32 v230, 63, v0
	v_lshrrev_b32_e32 v231, 6, v0
	v_lshrrev_b32_e32 v232, 4, v0
	v_mul_u32_u24_e32 v232, 0xe00, v232
	v_and_b32_e32 v233, 15, v0
	v_lshl_add_u32 v232, v233, 4, v232
	v_sub_u32_e32 v232, v186, v232
	v_lshrrev_b32_e32 v233, 3, v0
	v_and_b32_e32 v236, 7, v0
	v_lshlrev_b32_e32 v236, 4, v236
	v_lshl_add_u32 v233, v233, 7, v236
	v_sub_u32_e32 v233, v182, v233
	v_add_u32_e32 v232, 0x39d1dc00, v232
	v_add_u32_e32 v233, 0x39b15600, v233
	v_mov_b32_e32 v243, 0
	v_mov_b32_e32 v244, 0x2000
	v_mov_b32_e32 v245, 0x38000
	v_bfe_u32 v236, v230, 2, 3
	v_lshl_add_u32 v236, v231, 3, v236
	v_and_b32_e32 v237, 0xfffffff3, v236
	v_and_b32_e32 v238, 4, v236
	v_lshl_or_b32 v237, v238, 1, v237
	v_and_b32_e32 v238, 8, v236
	v_lshrrev_b32_e32 v238, 1, v238
	v_or_b32_e32 v237, v237, v238
	v_add_u32_e32 v237, 64, v237
	v_mul_u32_u24_e32 v237, 0xe00, v237
	v_add_u32_e32 v237, v237, v232
	v_lshrrev_b32_e32 v238, 5, v230
	v_lshlrev_b32_e32 v238, 6, v238
	v_and_b32_e32 v239, 3, v230
	v_lshl_add_u32 v238, v239, 4, v238
	v_add_u32_e32 v237, v237, v238
	v_add_u32_e32 v242, 0x100, v237
	v_lshl_add_u64 v[206:207], s[14:15], 0, v[242:243]
	v_mov_b32_e32 v236, v230
	v_mul_u32_u24_e32 v237, 0x2ab, v236
	v_lshrrev_b32_e32 v237, 14, v237
	v_mul_u32_u24_e32 v238, 24, v237
	v_sub_u32_e32 v238, v236, v238
	v_lshl_add_u32 v237, v231, 3, v237
	v_bfe_u32 v239, v237, 1, 3
	v_xor_b32_e32 v238, v238, v239
	v_add_u32_e32 v237, 0x80, v237
	v_mul_u32_u24_e32 v240, 0xe00, v237
	v_add_u32_e32 v240, v240, v232
	v_lshl_add_u32 v240, v238, 4, v240
	v_lshl_add_u32 v241, v237, 7, v233
	v_lshl_add_u32 v241, v238, 4, v241
	v_subrev_u32_e32 v241, 0x100, v241
	v_cmp_gt_u32_e32 vcc, 16, v238
	s_nop 1
	v_cndmask_b32_e32 v242, v241, v240, vcc
	v_cndmask_b32_e32 v205, v244, v245, vcc
	v_lshl_add_u64 v[182:183], s[14:15], 0, v[242:243]
	v_add_u32_e32 v236, 0x40, v230
	v_mul_u32_u24_e32 v237, 0x2ab, v236
	v_lshrrev_b32_e32 v237, 14, v237
	v_mul_u32_u24_e32 v238, 24, v237
	v_sub_u32_e32 v238, v236, v238
	v_lshl_add_u32 v237, v231, 3, v237
	v_bfe_u32 v239, v237, 1, 3
	v_xor_b32_e32 v238, v238, v239
	v_add_u32_e32 v237, 0x80, v237
	v_mul_u32_u24_e32 v240, 0xe00, v237
	v_add_u32_e32 v240, v240, v232
	v_lshl_add_u32 v240, v238, 4, v240
	v_lshl_add_u32 v241, v237, 7, v233
	v_lshl_add_u32 v241, v238, 4, v241
	v_subrev_u32_e32 v241, 0x100, v241
	v_cmp_gt_u32_e32 vcc, 16, v238
	s_nop 1
	v_cndmask_b32_e32 v242, v241, v240, vcc
	v_cndmask_b32_e32 v208, v244, v245, vcc
	v_lshl_add_u64 v[184:185], s[14:15], 0, v[242:243]
	v_add_u32_e32 v236, 0x80, v230
	v_mul_u32_u24_e32 v237, 0x2ab, v236
	v_lshrrev_b32_e32 v237, 14, v237
	v_mul_u32_u24_e32 v238, 24, v237
	v_sub_u32_e32 v238, v236, v238
	v_lshl_add_u32 v237, v231, 3, v237
	v_bfe_u32 v239, v237, 1, 3
	v_xor_b32_e32 v238, v238, v239
	v_add_u32_e32 v237, 0x80, v237
	v_mul_u32_u24_e32 v240, 0xe00, v237
	v_add_u32_e32 v240, v240, v232
	v_lshl_add_u32 v240, v238, 4, v240
	v_lshl_add_u32 v241, v237, 7, v233
	v_lshl_add_u32 v241, v238, 4, v241
	v_subrev_u32_e32 v241, 0x100, v241
	v_cmp_gt_u32_e32 vcc, 16, v238
	s_nop 1
	v_cndmask_b32_e32 v242, v241, v240, vcc
	v_cndmask_b32_e32 v209, v244, v245, vcc
	v_lshl_add_u64 v[186:187], s[14:15], 0, v[242:243]
	v_lshrrev_b32_e32 v236, 8, v0
	s_nop 0
	v_readfirstlane_b32 s98, v236
.LBB0_1344:
	s_cmp_eq_u32 s98, 0
	s_cbranch_scc1 .Latt_p0a
	v_readfirstlane_b32 s4, v0
	s_nop 0
	s_lshl_b32 s5, s4, 4
	s_mul_i32 s4, s5, 3
	s_add_i32 m0, s4, 0x8000
	s_nop 0
	global_load_lds_dwordx4 v[182:183], off
	s_add_i32 m0, s4, 0x8400
	s_nop 0
	global_load_lds_dwordx4 v[184:185], off
	s_add_i32 m0, s4, 0x8800
	s_nop 0
	global_load_lds_dwordx4 v[186:187], off
	s_lshl_b32 s5, s5, 1
	s_add_i32 m0, s5, 0x4000
	s_nop 0
	global_load_lds_dwordx4 v[206:207], off
	s_add_i32 m0, s5, 0x4380
	s_nop 0
	global_load_lds_dwordx4 v[206:207], off offset:128
	v_add_co_u32_e32 v182, vcc, v182, v205
	s_nop 1
	v_addc_co_u32_e32 v183, vcc, 0, v183, vcc
	v_add_co_u32_e32 v184, vcc, v184, v208
	s_nop 1
	v_addc_co_u32_e32 v185, vcc, 0, v185, vcc
	v_add_co_u32_e32 v186, vcc, v186, v209
	s_nop 1
	v_addc_co_u32_e32 v187, vcc, 0, v187, vcc
	v_add_co_u32_e32 v206, vcc, 0x38000, v206
	s_nop 1
	v_addc_co_u32_e32 v207, vcc, 0, v207, vcc
.Latt_p0a:
	ds_read_b128 v[230:233], v203 offset:24576
	ds_read_b128 v[236:239], v203 offset:36864
	ds_read_b128 v[240:243], v204 offset:24576
	ds_read_b128 v[244:247], v204 offset:36864
	ds_read_b128 v[66:69], v201 offset:36864
	ds_read_b128 v[70:73], v201 offset:24576
	ds_read_b128 v[212:215], v202 offset:24576
	ds_read_b128 v[216:219], v202 offset:36864
	v_add_f32_e32 v168, 0, v169
	v_add_f32_e32 v168, v191, v168
	v_add_f32_e32 v168, v170, v168
	s_waitcnt lgkmcnt(2)
	v_mfma_f32_32x32x16_bf16 v[82:97], v[70:73], v[128:131], 0
	v_add_f32_e32 v168, v192, v168
	v_add_f32_e32 v168, v190, v168
	v_add_f32_e32 v168, v193, v168
	v_add_f32_e32 v168, v171, v168
	v_add_f32_e32 v168, v189, v168
	v_add_f32_e32 v168, v173, v168
	v_add_f32_e32 v168, v175, v168
	v_mfma_f32_32x32x16_bf16 v[66:81], v[66:69], v[128:131], 0
	v_add_f32_e32 v168, v174, v168
	v_add_f32_e32 v168, v188, v168
	v_exp_f32_e32 v162, v162
	v_add_f32_e32 v168, v164, v168
	v_exp_f32_e32 v163, v163
	v_add_f32_e32 v168, v166, v168
	v_exp_f32_e32 v160, v160
	v_mfma_f32_32x32x16_bf16 v[82:97], v[230:233], v[124:127], v[82:97]
	v_add_f32_e32 v168, v165, v168
	v_exp_f32_e32 v161, v161
	v_add_f32_e32 v168, v167, v168
	v_exp_f32_e32 v156, v156
	v_add_f32_e32 v168, v162, v168
	v_exp_f32_e32 v157, v157
	v_add_f32_e32 v168, v163, v168
	v_mfma_f32_32x32x16_bf16 v[66:81], v[236:239], v[124:127], v[66:81]
	ds_read_b128 v[230:233], v201 offset:24704
	ds_read_b128 v[236:239], v201 offset:36992
	v_exp_f32_e32 v152, v152
	v_add_f32_e32 v168, v160, v168
	v_exp_f32_e32 v153, v153
	v_add_f32_e32 v168, v161, v168
	v_exp_f32_e32 v150, v150
	v_add_f32_e32 v168, v156, v168
	v_mfma_f32_32x32x16_bf16 v[82:97], v[240:243], v[120:123], v[82:97]
	v_exp_f32_e32 v151, v151
	v_add_f32_e32 v168, v157, v168
	v_exp_f32_e32 v158, v158
	v_add_f32_e32 v168, v152, v168
	v_exp_f32_e32 v159, v159
	v_add_f32_e32 v168, v153, v168
	v_exp_f32_e32 v154, v154
	v_mfma_f32_32x32x16_bf16 v[66:81], v[244:247], v[120:123], v[66:81]
	ds_read_b128 v[240:243], v203 offset:24704
	ds_read_b128 v[244:247], v203 offset:36992
	v_add_f32_e32 v168, v150, v168
	v_exp_f32_e32 v155, v155
	v_add_f32_e32 v168, v151, v168
	v_exp_f32_e32 v148, v148
	v_add_f32_e32 v168, v158, v168
	v_exp_f32_e32 v149, v149
	s_waitcnt lgkmcnt(5)
	v_mfma_f32_32x32x16_bf16 v[82:97], v[212:215], v[116:119], v[82:97]
	v_add_f32_e32 v168, v159, v168
	v_add_f32_e32 v168, v154, v168
	v_add_f32_e32 v168, v155, v168
	v_add_f32_e32 v168, v148, v168
	s_waitcnt lgkmcnt(4)
	v_mfma_f32_32x32x16_bf16 v[66:81], v[216:219], v[116:119], v[66:81]
	ds_read_b128 v[212:215], v204 offset:24704
	ds_read_b128 v[216:219], v204 offset:36992
	s_waitcnt lgkmcnt(5)
	v_mfma_f32_32x32x16_bf16 v[82:97], v[230:233], v[112:115], v[82:97]
	s_waitcnt lgkmcnt(4)
	v_mfma_f32_32x32x16_bf16 v[66:81], v[236:239], v[112:115], v[66:81]
	ds_read_b128 v[230:233], v202 offset:24704
	ds_read_b128 v[236:239], v202 offset:36992
	s_waitcnt lgkmcnt(5)
	v_mfma_f32_32x32x16_bf16 v[82:97], v[240:243], v[108:111], v[82:97]
	s_waitcnt lgkmcnt(4)
	v_mfma_f32_32x32x16_bf16 v[66:81], v[244:247], v[108:111], v[66:81]
	ds_read_b128 v[240:243], v201 offset:24832
	ds_read_b128 v[244:247], v201 offset:37120
	s_waitcnt lgkmcnt(5)
	v_mfma_f32_32x32x16_bf16 v[82:97], v[212:215], v[104:107], v[82:97]
	s_waitcnt lgkmcnt(4)
	v_mfma_f32_32x32x16_bf16 v[66:81], v[216:219], v[104:107], v[66:81]
	ds_read_b128 v[212:215], v203 offset:24832
	ds_read_b128 v[216:219], v203 offset:37120
	s_waitcnt lgkmcnt(5)
	v_mfma_f32_32x32x16_bf16 v[82:97], v[230:233], v[100:103], v[82:97]
	s_waitcnt lgkmcnt(4)
	v_mfma_f32_32x32x16_bf16 v[66:81], v[236:239], v[100:103], v[66:81]
	ds_read_b128 v[230:233], v204 offset:24832
	ds_read_b128 v[236:239], v204 offset:37120
	s_waitcnt lgkmcnt(5)
	v_mfma_f32_32x32x16_bf16 v[82:97], v[240:243], v[144:147], v[82:97]
	s_waitcnt lgkmcnt(4)
	v_mfma_f32_32x32x16_bf16 v[66:81], v[244:247], v[144:147], v[66:81]
	ds_read_b128 v[240:243], v202 offset:24832
	ds_read_b128 v[244:247], v202 offset:37120
	s_waitcnt lgkmcnt(5)
	v_mfma_f32_32x32x16_bf16 v[82:97], v[212:215], v[140:143], v[82:97]
	v_add_f32_e32 v212, v149, v168
	v_mov_b32_e32 v213, v212
	v_cvt_pk_bf16_f32 v168, v169, v191
	v_cvt_pk_bf16_f32 v169, v170, v192
	v_cvt_pk_bf16_f32 v170, v190, v193
	v_cvt_pk_bf16_f32 v171, v171, v189
	v_cvt_pk_bf16_f32 v172, v173, v175
	s_waitcnt lgkmcnt(4)
	v_mfma_f32_32x32x16_bf16 v[66:81], v[216:219], v[140:143], v[66:81]
	v_cvt_pk_bf16_f32 v173, v174, v188
	v_cvt_pk_bf16_f32 v174, v164, v166
	v_permlane32_swap_b32_e32 v212, v213
	v_permlane32_swap_b32_e32 v168, v170
	v_cvt_pk_bf16_f32 v175, v165, v167
	s_waitcnt lgkmcnt(3)
	v_mfma_f32_32x32x16_bf16 v[82:97], v[230:233], v[136:139], v[82:97]
	v_permlane32_swap_b32_e32 v172, v174
	v_cvt_pk_bf16_f32 v214, v162, v163
	v_cvt_pk_bf16_f32 v215, v160, v161
	v_cvt_pk_bf16_f32 v216, v156, v157
	v_cvt_pk_bf16_f32 v217, v152, v153
	v_cvt_pk_bf16_f32 v230, v150, v151
	s_waitcnt lgkmcnt(2)
	v_mfma_f32_32x32x16_bf16 v[66:81], v[236:239], v[136:139], v[66:81]
	v_cvt_pk_bf16_f32 v231, v158, v159
	v_cvt_pk_bf16_f32 v232, v154, v155
	v_cvt_pk_bf16_f32 v233, v148, v149
	v_permlane32_swap_b32_e32 v169, v171
	v_permlane32_swap_b32_e32 v173, v175
	s_waitcnt lgkmcnt(1)
	v_mfma_f32_32x32x16_bf16 v[82:97], v[240:243], v[132:135], v[82:97]
	v_permlane32_swap_b32_e32 v214, v216
	v_permlane32_swap_b32_e32 v215, v217
	v_permlane32_swap_b32_e32 v230, v232
	v_permlane32_swap_b32_e32 v231, v233
	s_waitcnt lgkmcnt(0)
	v_mfma_f32_32x32x16_bf16 v[66:81], v[244:247], v[132:135], v[66:81]
	s_cmp_lg_u32 s98, 0
	s_cbranch_scc1 .Latt_p1a
	v_readfirstlane_b32 s4, v0
	s_nop 0
	s_lshl_b32 s5, s4, 4
	s_mul_i32 s4, s5, 3
	s_add_i32 m0, s4, 0x8000
	s_nop 0
	global_load_lds_dwordx4 v[182:183], off
	s_add_i32 m0, s4, 0x8400
	s_nop 0
	global_load_lds_dwordx4 v[184:185], off
	s_add_i32 m0, s4, 0x8800
	s_nop 0
	global_load_lds_dwordx4 v[186:187], off
	s_lshl_b32 s5, s5, 1
	s_add_i32 m0, s5, 0x4000
	s_nop 0
	global_load_lds_dwordx4 v[206:207], off
	s_add_i32 m0, s5, 0x4380
	s_nop 0
	global_load_lds_dwordx4 v[206:207], off offset:128
	v_add_co_u32_e32 v182, vcc, v182, v205
	s_nop 1
	v_addc_co_u32_e32 v183, vcc, 0, v183, vcc
	v_add_co_u32_e32 v184, vcc, v184, v208
	s_nop 1
	v_addc_co_u32_e32 v185, vcc, 0, v185, vcc
	v_add_co_u32_e32 v186, vcc, v186, v209
	s_nop 1
	v_addc_co_u32_e32 v187, vcc, 0, v187, vcc
	v_add_co_u32_e32 v206, vcc, 0x38000, v206
	s_nop 1
	v_addc_co_u32_e32 v207, vcc, 0, v207, vcc
.Latt_p1a:
	ds_read_b64_tr_b16 v[236:237], v200 offset:0
	ds_read_b64_tr_b16 v[238:239], v200 offset:0x800
	ds_read_b64_tr_b16 v[240:241], v200 offset:0x1000
	ds_read_b64_tr_b16 v[242:243], v200 offset:0x1800
	ds_read_b64_tr_b16 v[244:245], v200 offset:0x2000
	ds_read_b64_tr_b16 v[246:247], v200 offset:0x2800
	ds_read_b64_tr_b16 v[222:223], v200 offset:0x3000
	ds_read_b64_tr_b16 v[224:225], v200 offset:0x3800
	s_waitcnt lgkmcnt(0)
	s_nop 0
	v_mfma_f32_32x32x16_bf16 v[2:17], v[168:171], v[236:239], v[2:17]
	v_mfma_f32_32x32x16_bf16 v[2:17], v[172:175], v[240:243], v[2:17]
	v_mfma_f32_32x32x16_bf16 v[2:17], v[214:217], v[244:247], v[2:17]
	v_mfma_f32_32x32x16_bf16 v[2:17], v[230:233], v[222:225], v[2:17]
	ds_read_b64_tr_b16 v[222:223], v200 offset:0x200
	ds_read_b64_tr_b16 v[224:225], v200 offset:0xa00
	ds_read_b64_tr_b16 v[236:237], v200 offset:0x1200
	ds_read_b64_tr_b16 v[238:239], v200 offset:0x1a00
	ds_read_b64_tr_b16 v[240:241], v200 offset:0x2200
	ds_read_b64_tr_b16 v[242:243], v200 offset:0x2a00
	ds_read_b64_tr_b16 v[244:245], v200 offset:0x3200
	ds_read_b64_tr_b16 v[246:247], v200 offset:0x3a00
	s_waitcnt lgkmcnt(0)
	s_nop 0
	v_mfma_f32_32x32x16_bf16 v[50:65], v[168:171], v[222:225], v[50:65]
	ds_read_b64_tr_b16 v[222:223], v200 offset:0x400
	ds_read_b64_tr_b16 v[224:225], v200 offset:0xc00
	v_mfma_f32_32x32x16_bf16 v[50:65], v[172:175], v[236:239], v[50:65]
	ds_read_b64_tr_b16 v[236:237], v200 offset:0x1400
	ds_read_b64_tr_b16 v[238:239], v200 offset:0x1c00
	v_mfma_f32_32x32x16_bf16 v[50:65], v[214:217], v[240:243], v[50:65]
	ds_read_b64_tr_b16 v[240:241], v200 offset:0x2400
	ds_read_b64_tr_b16 v[242:243], v200 offset:0x2c00
	v_mfma_f32_32x32x16_bf16 v[50:65], v[230:233], v[244:247], v[50:65]
	ds_read_b64_tr_b16 v[244:245], v200 offset:0x3400
	ds_read_b64_tr_b16 v[246:247], v200 offset:0x3c00
	s_waitcnt lgkmcnt(0)
	v_mfma_f32_32x32x16_bf16 v[34:49], v[168:171], v[222:225], v[34:49]
	ds_read_b64_tr_b16 v[222:223], v200 offset:0x600
	ds_read_b64_tr_b16 v[224:225], v200 offset:0xe00
	v_mfma_f32_32x32x16_bf16 v[34:49], v[172:175], v[236:239], v[34:49]
	ds_read_b64_tr_b16 v[236:237], v200 offset:0x1600
	ds_read_b64_tr_b16 v[238:239], v200 offset:0x1e00
	v_mfma_f32_32x32x16_bf16 v[34:49], v[214:217], v[240:243], v[34:49]
	ds_read_b64_tr_b16 v[240:241], v200 offset:0x2600
	ds_read_b64_tr_b16 v[242:243], v200 offset:0x2e00
	v_mfma_f32_32x32x16_bf16 v[34:49], v[230:233], v[244:247], v[34:49]
	ds_read_b64_tr_b16 v[244:245], v200 offset:0x3600
	ds_read_b64_tr_b16 v[246:247], v200 offset:0x3e00
	s_waitcnt lgkmcnt(0)
	s_cmp_eq_u32 s98, 0
	s_cbranch_scc1 .Latt_p2a
	s_waitcnt vmcnt(0)
	s_barrier
.Latt_p2a:
	v_mfma_f32_32x32x16_bf16 v[18:33], v[168:171], v[222:225], v[18:33]
	v_max_f32_e32 v168, v83, v83
	v_max_f32_e32 v169, v82, v82
	v_max_f32_e32 v168, v169, v168
	v_max3_f32 v168, v168, v84, v85
	v_max3_f32 v168, v168, v86, v87
	v_max3_f32 v168, v168, v88, v89
	v_max3_f32 v168, v168, v90, v91
	v_max3_f32 v168, v168, v92, v93
	v_max3_f32 v168, v168, v94, v95
	v_mfma_f32_32x32x16_bf16 v[18:33], v[172:175], v[236:239], v[18:33]
	v_max3_f32 v168, v168, v96, v97
	v_max3_f32 v168, v168, v66, v67
	v_max3_f32 v168, v168, v68, v69
	v_max3_f32 v168, v168, v70, v71
	v_max3_f32 v168, v168, v72, v73
	v_max3_f32 v168, v168, v74, v75
	v_max3_f32 v168, v168, v76, v77
	v_max3_f32 v168, v168, v78, v79
	v_mfma_f32_32x32x16_bf16 v[18:33], v[214:217], v[240:243], v[18:33]
	v_max3_f32 v168, v168, v80, v81
	v_mov_b32_e32 v169, v168
	s_nop 1
	v_permlane32_swap_b32_e32 v168, v169
	v_max_f32_e32 v169, v169, v169
	v_max_f32_e32 v168, v168, v168
	v_max_f32_e32 v168, v168, v169
	v_sub_f32_e32 v169, v168, v211
	v_cmp_ge_f32_e32 vcc, s11, v169
	v_max_f32_e32 v169, v211, v211
	v_max_f32_e32 v168, v169, v168
	v_mfma_f32_32x32x16_bf16 v[18:33], v[230:233], v[244:247], v[18:33]
	v_sub_f32_e32 v169, v211, v168
	v_mul_f32_e32 v169, 0x3dd53b94, v169
	v_exp_f32_e32 v169, v169
	s_cmp_eq_u64 vcc, exec
	s_cselect_b64 s[18:19], -1, 0
	v_cndmask_b32_e64 v172, v169, 1.0, s[18:19]
	v_cmp_gt_f32_e32 vcc, 1.0, v172
	s_cbranch_vccz .LBB0_1348
	s_and_saveexec_b64 s[4:5], s[0:1]
	ds_write_b32 v197, v172 offset:128
	s_or_b64 exec, exec, s[4:5]
	s_waitcnt lgkmcnt(0)
	v_add_u32_e32 v160, v196, v98
	ds_read_b128 v[148:151], v160 offset:224
	ds_read_b128 v[152:155], v160 offset:192
	ds_read_b128 v[156:159], v160 offset:160
	ds_read_b128 v[160:163], v160 offset:128
	v_mov_b32_e32 v228, 0xffffce00
	s_waitcnt lgkmcnt(3)
	v_pk_mul_f32 v[14:15], v[14:15], v[148:149]
	s_waitcnt lgkmcnt(2)
	v_pk_mul_f32 v[10:11], v[10:11], v[152:153]
	s_waitcnt lgkmcnt(1)
	v_pk_mul_f32 v[6:7], v[6:7], v[156:157]
	v_pk_mul_f32 v[16:17], v[16:17], v[150:151]
	v_pk_mul_f32 v[12:13], v[12:13], v[154:155]
	v_pk_mul_f32 v[8:9], v[8:9], v[158:159]
	s_waitcnt lgkmcnt(0)
	v_pk_mul_f32 v[4:5], v[4:5], v[162:163]
	v_pk_mul_f32 v[2:3], v[2:3], v[160:161]
	v_pk_mul_f32 v[62:63], v[62:63], v[148:149]
	v_pk_mul_f32 v[58:59], v[58:59], v[152:153]
	v_pk_mul_f32 v[54:55], v[54:55], v[156:157]
	v_pk_mul_f32 v[64:65], v[64:65], v[150:151]
	v_pk_mul_f32 v[60:61], v[60:61], v[154:155]
	v_pk_mul_f32 v[56:57], v[56:57], v[158:159]
	v_pk_mul_f32 v[52:53], v[52:53], v[162:163]
	v_pk_mul_f32 v[50:51], v[50:51], v[160:161]
	v_pk_mul_f32 v[46:47], v[46:47], v[148:149]
	v_pk_mul_f32 v[42:43], v[42:43], v[152:153]
	v_pk_mul_f32 v[38:39], v[38:39], v[156:157]
	v_pk_mul_f32 v[48:49], v[48:49], v[150:151]
	v_pk_mul_f32 v[44:45], v[44:45], v[154:155]
	v_pk_mul_f32 v[40:41], v[40:41], v[158:159]
	v_pk_mul_f32 v[36:37], v[36:37], v[162:163]
	v_pk_mul_f32 v[34:35], v[34:35], v[160:161]
	v_pk_mul_f32 v[30:31], v[30:31], v[148:149]
	v_pk_mul_f32 v[26:27], v[26:27], v[152:153]
	v_pk_mul_f32 v[22:23], v[22:23], v[156:157]
	v_pk_mul_f32 v[32:33], v[32:33], v[150:151]
	v_pk_mul_f32 v[28:29], v[28:29], v[154:155]
	v_pk_mul_f32 v[24:25], v[24:25], v[158:159]
	v_pk_mul_f32 v[20:21], v[20:21], v[162:163]
	v_pk_mul_f32 v[18:19], v[18:19], v[160:161]
	s_branch .LBB0_1349

.LBB0_1349:
	v_cndmask_b32_e64 v173, v168, v211, s[18:19]
	v_mul_f32_e32 v164, 0xbdd53b94, v173
	v_fmamk_f32 v82, v82, 0x3dd53b94, v164
	v_fmamk_f32 v83, v83, 0x3dd53b94, v164
	v_fmamk_f32 v84, v84, 0x3dd53b94, v164
	v_fmamk_f32 v85, v85, 0x3dd53b94, v164
	v_fmamk_f32 v86, v86, 0x3dd53b94, v164
	v_fmamk_f32 v87, v87, 0x3dd53b94, v164
	v_fmamk_f32 v88, v88, 0x3dd53b94, v164
	v_fmamk_f32 v89, v89, 0x3dd53b94, v164
	v_fmamk_f32 v90, v90, 0x3dd53b94, v164
	v_fmamk_f32 v91, v91, 0x3dd53b94, v164
	v_fmamk_f32 v92, v92, 0x3dd53b94, v164
	v_fmamk_f32 v93, v93, 0x3dd53b94, v164
	v_fmamk_f32 v94, v94, 0x3dd53b94, v164
	v_fmamk_f32 v95, v95, 0x3dd53b94, v164
	v_fmamk_f32 v96, v96, 0x3dd53b94, v164
	v_fmamk_f32 v97, v97, 0x3dd53b94, v164
	v_fmamk_f32 v229, v68, 0x3dd53b94, v164
	v_fmamk_f32 v230, v69, 0x3dd53b94, v164
	v_fmamk_f32 v168, v73, 0x3dd53b94, v164
	v_fmamk_f32 v169, v74, 0x3dd53b94, v164
	v_fmamk_f32 v175, v66, 0x3dd53b94, v164
	v_fmamk_f32 v211, v67, 0x3dd53b94, v164
	v_fmamk_f32 v231, v70, 0x3dd53b94, v164
	v_fmamk_f32 v166, v71, 0x3dd53b94, v164
	v_fmamk_f32 v167, v72, 0x3dd53b94, v164
	v_fmamk_f32 v170, v75, 0x3dd53b94, v164
	v_fmamk_f32 v171, v76, 0x3dd53b94, v164
	v_fmamk_f32 v174, v77, 0x3dd53b94, v164
	v_fmamk_f32 v165, v78, 0x3dd53b94, v164
	v_exp_f32_e32 v161, v82
	v_exp_f32_e32 v163, v83
	v_exp_f32_e32 v159, v84
	v_exp_f32_e32 v162, v85
	v_exp_f32_e32 v158, v86
	v_exp_f32_e32 v160, v87
	v_exp_f32_e32 v156, v88
	v_exp_f32_e32 v157, v89
	v_exp_f32_e32 v153, v90
	v_exp_f32_e32 v155, v91
	v_exp_f32_e32 v152, v92
	v_exp_f32_e32 v154, v93
	v_exp_f32_e32 v149, v94
	v_exp_f32_e32 v151, v95
	v_exp_f32_e32 v148, v96
	v_exp_f32_e32 v150, v97
	v_fmamk_f32 v232, v79, 0x3dd53b94, v164
	v_fmamk_f32 v233, v80, 0x3dd53b94, v164
	v_fmac_f32_e32 v164, 0x3dd53b94, v81
	s_waitcnt lgkmcnt(0)
	s_cmp_lg_u32 s98, 0
	s_cbranch_scc1 .Latt_p3a
	s_waitcnt vmcnt(0)
	s_barrier
.Latt_p3a:
	s_cmp_eq_u32 s98, 0
	s_cbranch_scc1 .Latt_p0b
	v_readfirstlane_b32 s4, v0
	s_nop 0
	s_lshl_b32 s5, s4, 4
	s_mul_i32 s4, s5, 3
	s_add_i32 m0, s4, 0xe000
	s_nop 0
	global_load_lds_dwordx4 v[182:183], off
	s_add_i32 m0, s4, 0xe400
	s_nop 0
	global_load_lds_dwordx4 v[184:185], off
	s_add_i32 m0, s4, 0xe800
	s_nop 0
	global_load_lds_dwordx4 v[186:187], off
	s_lshl_b32 s5, s5, 1
	s_mov_b32 m0, s5
	s_nop 0
	global_load_lds_dwordx4 v[206:207], off
	s_add_i32 m0, s5, 0x380
	s_nop 0
	global_load_lds_dwordx4 v[206:207], off offset:128
	v_add_co_u32_e32 v182, vcc, v182, v205
	s_nop 1
	v_addc_co_u32_e32 v183, vcc, 0, v183, vcc
	v_add_co_u32_e32 v184, vcc, v184, v208
	s_nop 1
	v_addc_co_u32_e32 v185, vcc, 0, v185, vcc
	v_add_co_u32_e32 v186, vcc, v186, v209
	s_nop 1
	v_addc_co_u32_e32 v187, vcc, 0, v187, vcc
	v_add_co_u32_e32 v206, vcc, 0x38000, v206
	s_nop 1
	v_addc_co_u32_e32 v207, vcc, 0, v207, vcc
.Latt_p0b:
	ds_read_b128 v[214:217], v203
	ds_read_b128 v[222:225], v203 offset:12288
	ds_read_b128 v[236:239], v204
	ds_read_b128 v[240:243], v204 offset:12288
	ds_read_b128 v[66:69], v201 offset:12288
	ds_read_b128 v[70:73], v201
	ds_read_b128 v[244:247], v202
	ds_read_b128 v[176:179], v202 offset:12288
	v_exp_f32_e32 v166, v166
	v_exp_f32_e32 v167, v167
	v_exp_f32_e32 v218, v169
	s_waitcnt lgkmcnt(2)
	v_mfma_f32_32x32x16_bf16 v[82:97], v[70:73], v[128:131], 0
	v_exp_f32_e32 v219, v170
	v_exp_f32_e32 v165, v165
	v_exp_f32_e32 v164, v164
	v_mfma_f32_32x32x16_bf16 v[82:97], v[214:217], v[124:127], v[82:97]
	v_mfma_f32_32x32x16_bf16 v[82:97], v[236:239], v[120:123], v[82:97]
	v_mfma_f32_32x32x16_bf16 v[66:81], v[66:69], v[128:131], 0
	s_waitcnt lgkmcnt(1)
	v_mfma_f32_32x32x16_bf16 v[82:97], v[244:247], v[116:119], v[82:97]
	v_mfma_f32_32x32x16_bf16 v[66:81], v[222:225], v[124:127], v[66:81]
	ds_read_b128 v[214:217], v201 offset:128
	ds_read_b128 v[222:225], v201 offset:12416
	s_waitcnt lgkmcnt(1)
	v_mfma_f32_32x32x16_bf16 v[82:97], v[214:217], v[112:115], v[82:97]
	v_mfma_f32_32x32x16_bf16 v[66:81], v[240:243], v[120:123], v[66:81]
	ds_read_b128 v[236:239], v203 offset:128
	ds_read_b128 v[240:243], v203 offset:12416
	s_waitcnt lgkmcnt(1)
	v_mfma_f32_32x32x16_bf16 v[82:97], v[236:239], v[108:111], v[82:97]
	v_mfma_f32_32x32x16_bf16 v[66:81], v[176:179], v[116:119], v[66:81]
	ds_read_b128 v[176:179], v204 offset:128
	ds_read_b128 v[244:247], v204 offset:12416
	s_waitcnt lgkmcnt(1)
	v_mfma_f32_32x32x16_bf16 v[82:97], v[176:179], v[104:107], v[82:97]
	v_mfma_f32_32x32x16_bf16 v[66:81], v[222:225], v[112:115], v[66:81]
	ds_read_b128 v[214:217], v202 offset:128
	ds_read_b128 v[222:225], v202 offset:12416
	s_waitcnt lgkmcnt(1)
	v_mfma_f32_32x32x16_bf16 v[82:97], v[214:217], v[100:103], v[82:97]
	v_mfma_f32_32x32x16_bf16 v[66:81], v[240:243], v[108:111], v[66:81]
	ds_read_b128 v[236:239], v201 offset:256
	ds_read_b128 v[240:243], v201 offset:12544
	s_waitcnt lgkmcnt(1)
	v_mfma_f32_32x32x16_bf16 v[82:97], v[236:239], v[144:147], v[82:97]
	v_mfma_f32_32x32x16_bf16 v[66:81], v[244:247], v[104:107], v[66:81]
	ds_read_b128 v[176:179], v203 offset:256
	ds_read_b128 v[244:247], v203 offset:12544
	s_waitcnt lgkmcnt(1)
	v_mfma_f32_32x32x16_bf16 v[82:97], v[176:179], v[140:143], v[82:97]
	v_exp_f32_e32 v178, v175
	v_exp_f32_e32 v179, v211
	v_exp_f32_e32 v211, v229
	v_mfma_f32_32x32x16_bf16 v[66:81], v[222:225], v[100:103], v[66:81]
	ds_read_b128 v[214:217], v204 offset:256
	ds_read_b128 v[222:225], v204 offset:12544
	s_waitcnt lgkmcnt(1)
	v_mfma_f32_32x32x16_bf16 v[82:97], v[214:217], v[136:139], v[82:97]
	v_exp_f32_e32 v217, v168
	v_add_f32_e32 v168, 0, v161
	v_add_f32_e32 v168, v163, v168
	v_add_f32_e32 v168, v159, v168
	v_add_f32_e32 v168, v162, v168
	v_add_f32_e32 v168, v158, v168
	v_add_f32_e32 v168, v160, v168
	v_mfma_f32_32x32x16_bf16 v[66:81], v[240:243], v[144:147], v[66:81]
	v_add_f32_e32 v168, v156, v168
	v_add_f32_e32 v168, v157, v168
	v_add_f32_e32 v168, v153, v168
	v_add_f32_e32 v168, v155, v168
	v_add_f32_e32 v168, v152, v168
	v_add_f32_e32 v168, v154, v168
	v_add_f32_e32 v168, v149, v168
	v_mfma_f32_32x32x16_bf16 v[66:81], v[244:247], v[140:143], v[66:81]
	v_add_f32_e32 v168, v151, v168
	v_add_f32_e32 v168, v148, v168
	v_exp_f32_e32 v215, v230
	v_add_f32_e32 v168, v150, v168
	v_exp_f32_e32 v216, v231
	v_add_f32_e32 v168, v178, v168
	v_add_f32_e32 v168, v179, v168
	s_waitcnt lgkmcnt(0)
	v_mfma_f32_32x32x16_bf16 v[66:81], v[222:225], v[136:139], v[66:81]
	v_add_f32_e32 v168, v211, v168
	v_add_f32_e32 v168, v215, v168
	v_add_f32_e32 v168, v216, v168
	ds_read_b128 v[236:239], v202 offset:256
	ds_read_b128 v[240:243], v202 offset:12544
	v_add_f32_e32 v168, v166, v168
	v_exp_f32_e32 v223, v171
	v_add_f32_e32 v168, v167, v168
	v_exp_f32_e32 v224, v174
	v_add_f32_e32 v168, v217, v168
	v_add_f32_e32 v168, v218, v168
	v_exp_f32_e32 v225, v232
	v_add_f32_e32 v168, v219, v168
	s_waitcnt lgkmcnt(1)
	v_mfma_f32_32x32x16_bf16 v[82:97], v[236:239], v[132:135], v[82:97]
	v_exp_f32_e32 v231, v233
	v_add_f32_e32 v168, v223, v168
	v_add_f32_e32 v168, v224, v168
	v_add_f32_e32 v168, v165, v168
	v_add_f32_e32 v168, v225, v168
	v_add_f32_e32 v168, v231, v168
	v_add_f32_e32 v229, v164, v168
	s_waitcnt lgkmcnt(0)
	v_mfma_f32_32x32x16_bf16 v[66:81], v[240:243], v[132:135], v[66:81]
	v_mov_b32_e32 v230, v229
	v_cvt_pk_bf16_f32 v168, v161, v163
	v_cvt_pk_bf16_f32 v169, v159, v162
	v_cvt_pk_bf16_f32 v170, v158, v160
	v_cvt_pk_bf16_f32 v171, v156, v157
	s_nop 1
	v_permlane32_swap_b32_e32 v229, v230
	v_permlane32_swap_b32_e32 v168, v170
	v_permlane32_swap_b32_e32 v169, v171
	v_cvt_pk_bf16_f32 v174, v153, v155
	v_cvt_pk_bf16_f32 v175, v152, v154
	v_cvt_pk_bf16_f32 v176, v149, v151
	v_cvt_pk_bf16_f32 v177, v148, v150
	v_cvt_pk_bf16_f32 v214, v178, v179
	v_cvt_pk_bf16_f32 v215, v211, v215
	v_cvt_pk_bf16_f32 v216, v216, v166
	v_cvt_pk_bf16_f32 v217, v167, v217
	v_cvt_pk_bf16_f32 v222, v218, v219
	v_cvt_pk_bf16_f32 v223, v223, v224
	v_cvt_pk_bf16_f32 v224, v165, v225
	v_cvt_pk_bf16_f32 v225, v231, v164
	s_nop 0
	v_permlane32_swap_b32_e32 v174, v176
	v_permlane32_swap_b32_e32 v175, v177
	v_permlane32_swap_b32_e32 v214, v216
	v_permlane32_swap_b32_e32 v215, v217
	v_permlane32_swap_b32_e32 v222, v224
	v_permlane32_swap_b32_e32 v223, v225
	s_cmp_lg_u32 s98, 0
	s_cbranch_scc1 .Latt_p1b
	v_readfirstlane_b32 s4, v0
	s_nop 0
	s_lshl_b32 s5, s4, 4
	s_mul_i32 s4, s5, 3
	s_add_i32 m0, s4, 0xe000
	s_nop 0
	global_load_lds_dwordx4 v[182:183], off
	s_add_i32 m0, s4, 0xe400
	s_nop 0
	global_load_lds_dwordx4 v[184:185], off
	s_add_i32 m0, s4, 0xe800
	s_nop 0
	global_load_lds_dwordx4 v[186:187], off
	s_lshl_b32 s5, s5, 1
	s_mov_b32 m0, s5
	s_nop 0
	global_load_lds_dwordx4 v[206:207], off
	s_add_i32 m0, s5, 0x380
	s_nop 0
	global_load_lds_dwordx4 v[206:207], off offset:128
	v_add_co_u32_e32 v182, vcc, v182, v205
	s_nop 1
	v_addc_co_u32_e32 v183, vcc, 0, v183, vcc
	v_add_co_u32_e32 v184, vcc, v184, v208
	s_nop 1
	v_addc_co_u32_e32 v185, vcc, 0, v185, vcc
	v_add_co_u32_e32 v186, vcc, v186, v209
	s_nop 1
	v_addc_co_u32_e32 v187, vcc, 0, v187, vcc
	v_add_co_u32_e32 v206, vcc, 0x38000, v206
	s_nop 1
	v_addc_co_u32_e32 v207, vcc, 0, v207, vcc
.Latt_p1b:
	ds_read_b64_tr_b16 v[188:189], v198 offset:0
	ds_read_b64_tr_b16 v[190:191], v198 offset:0x800
	ds_read_b64_tr_b16 v[236:237], v198 offset:0x1000
	ds_read_b64_tr_b16 v[238:239], v198 offset:0x1800
	ds_read_b64_tr_b16 v[240:241], v198 offset:0x2000
	ds_read_b64_tr_b16 v[242:243], v198 offset:0x2800
	ds_read_b64_tr_b16 v[244:245], v198 offset:0x3000
	ds_read_b64_tr_b16 v[246:247], v198 offset:0x3800
	s_waitcnt lgkmcnt(0)
	s_nop 0
	v_mfma_f32_32x32x16_bf16 v[2:17], v[168:171], v[188:191], v[2:17]
	ds_read_b64_tr_b16 v[188:189], v198 offset:0x200
	ds_read_b64_tr_b16 v[190:191], v198 offset:0xa00
	v_mfma_f32_32x32x16_bf16 v[2:17], v[174:177], v[236:239], v[2:17]
	ds_read_b64_tr_b16 v[236:237], v198 offset:0x1200
	ds_read_b64_tr_b16 v[238:239], v198 offset:0x1a00
	v_mfma_f32_32x32x16_bf16 v[2:17], v[214:217], v[240:243], v[2:17]
	ds_read_b64_tr_b16 v[240:241], v198 offset:0x2200
	ds_read_b64_tr_b16 v[242:243], v198 offset:0x2a00
	v_mfma_f32_32x32x16_bf16 v[2:17], v[222:225], v[244:247], v[2:17]
	ds_read_b64_tr_b16 v[244:245], v198 offset:0x3200
	ds_read_b64_tr_b16 v[246:247], v198 offset:0x3a00
	s_waitcnt lgkmcnt(0)
	v_mfma_f32_32x32x16_bf16 v[50:65], v[168:171], v[188:191], v[50:65]
	ds_read_b64_tr_b16 v[188:189], v198 offset:0x400
	ds_read_b64_tr_b16 v[190:191], v198 offset:0xc00
	v_mfma_f32_32x32x16_bf16 v[50:65], v[174:177], v[236:239], v[50:65]
	ds_read_b64_tr_b16 v[236:237], v198 offset:0x1400
	ds_read_b64_tr_b16 v[238:239], v198 offset:0x1c00
	v_mfma_f32_32x32x16_bf16 v[50:65], v[214:217], v[240:243], v[50:65]
	ds_read_b64_tr_b16 v[240:241], v198 offset:0x2400
	ds_read_b64_tr_b16 v[242:243], v198 offset:0x2c00
	v_mfma_f32_32x32x16_bf16 v[50:65], v[222:225], v[244:247], v[50:65]
	ds_read_b64_tr_b16 v[244:245], v198 offset:0x3400
	ds_read_b64_tr_b16 v[246:247], v198 offset:0x3c00
	s_waitcnt lgkmcnt(0)
	v_mfma_f32_32x32x16_bf16 v[34:49], v[168:171], v[188:191], v[34:49]
	ds_read_b64_tr_b16 v[188:189], v198 offset:0x600
	ds_read_b64_tr_b16 v[190:191], v198 offset:0xe00
	v_mfma_f32_32x32x16_bf16 v[34:49], v[174:177], v[236:239], v[34:49]
	ds_read_b64_tr_b16 v[236:237], v198 offset:0x1600
	ds_read_b64_tr_b16 v[238:239], v198 offset:0x1e00
	v_mfma_f32_32x32x16_bf16 v[34:49], v[214:217], v[240:243], v[34:49]
	ds_read_b64_tr_b16 v[240:241], v198 offset:0x2600
	ds_read_b64_tr_b16 v[242:243], v198 offset:0x2e00
	v_mfma_f32_32x32x16_bf16 v[34:49], v[222:225], v[244:247], v[34:49]
	ds_read_b64_tr_b16 v[244:245], v198 offset:0x3600
	ds_read_b64_tr_b16 v[246:247], v198 offset:0x3e00
	s_waitcnt lgkmcnt(0)
	s_cmp_eq_u32 s98, 0
	s_cbranch_scc1 .Latt_p2b
	s_waitcnt vmcnt(0)
	s_barrier
.Latt_p2b:
	v_mfma_f32_32x32x16_bf16 v[18:33], v[168:171], v[188:191], v[18:33]
	v_max_f32_e32 v168, v83, v83
	v_max_f32_e32 v169, v82, v82
	v_max_f32_e32 v168, v169, v168
	v_max3_f32 v168, v168, v84, v85
	v_max3_f32 v168, v168, v86, v87
	v_max3_f32 v168, v168, v88, v89
	v_max3_f32 v168, v168, v90, v91
	v_max3_f32 v168, v168, v92, v93
	v_max3_f32 v168, v168, v94, v95
	v_mfma_f32_32x32x16_bf16 v[18:33], v[174:177], v[236:239], v[18:33]
	v_max3_f32 v168, v168, v96, v97
	v_max3_f32 v168, v168, v66, v67
	v_max3_f32 v168, v168, v68, v69
	v_max3_f32 v168, v168, v70, v71
	v_max3_f32 v168, v168, v72, v73
	v_max3_f32 v168, v168, v74, v75
	v_max3_f32 v168, v168, v76, v77
	v_max3_f32 v168, v168, v78, v79
	v_mfma_f32_32x32x16_bf16 v[18:33], v[214:217], v[240:243], v[18:33]
	v_max3_f32 v168, v168, v80, v81
	v_mov_b32_e32 v169, v168
	s_nop 1
	v_permlane32_swap_b32_e32 v168, v169
	v_max_f32_e32 v169, v169, v169
	v_max_f32_e32 v168, v168, v168
	v_max_f32_e32 v168, v168, v169
	v_sub_f32_e32 v169, v168, v173
	v_cmp_ge_f32_e32 vcc, s11, v169
	v_max_f32_e32 v169, v173, v173
	v_max_f32_e32 v169, v169, v168
	v_mfma_f32_32x32x16_bf16 v[18:33], v[222:225], v[244:247], v[18:33]
	v_sub_f32_e32 v168, v173, v169
	v_mul_f32_e32 v168, 0x3dd53b94, v168
	v_exp_f32_e32 v168, v168
	s_cmp_eq_u64 vcc, exec
	s_cselect_b64 s[18:19], -1, 0
	v_cndmask_b32_e64 v168, v168, 1.0, s[18:19]
	v_cmp_gt_f32_e32 vcc, 1.0, v168
	s_cbranch_vccz .LBB0_1353
	s_mov_b64 s[4:5], exec
	s_and_b64 s[22:23], s[4:5], s[0:1]
	v_mov_b32_e32 v246, v227
	s_mov_b64 exec, s[22:23]
	ds_write_b32 v197, v168 offset:128
	s_or_b64 exec, exec, s[4:5]
	s_waitcnt lgkmcnt(0)
	v_add_u32_e32 v160, v196, v98
	ds_read_b128 v[148:151], v160 offset:224
	ds_read_b128 v[152:155], v160 offset:192
	ds_read_b128 v[156:159], v160 offset:160
	ds_read_b128 v[160:163], v160 offset:128
	s_waitcnt lgkmcnt(3)
	v_pk_mul_f32 v[14:15], v[14:15], v[148:149]
	s_waitcnt lgkmcnt(2)
	v_pk_mul_f32 v[10:11], v[10:11], v[152:153]
	s_waitcnt lgkmcnt(1)
	v_pk_mul_f32 v[6:7], v[6:7], v[156:157]
	v_pk_mul_f32 v[16:17], v[16:17], v[150:151]
	v_pk_mul_f32 v[12:13], v[12:13], v[154:155]
	v_pk_mul_f32 v[8:9], v[8:9], v[158:159]
	s_waitcnt lgkmcnt(0)
	v_pk_mul_f32 v[4:5], v[4:5], v[162:163]
	v_pk_mul_f32 v[2:3], v[2:3], v[160:161]
	v_pk_mul_f32 v[62:63], v[62:63], v[148:149]
	v_pk_mul_f32 v[58:59], v[58:59], v[152:153]
	v_pk_mul_f32 v[54:55], v[54:55], v[156:157]
	v_pk_mul_f32 v[64:65], v[64:65], v[150:151]
	v_pk_mul_f32 v[60:61], v[60:61], v[154:155]
	v_pk_mul_f32 v[56:57], v[56:57], v[158:159]
	v_pk_mul_f32 v[52:53], v[52:53], v[162:163]
	v_pk_mul_f32 v[50:51], v[50:51], v[160:161]
	v_pk_mul_f32 v[46:47], v[46:47], v[148:149]
	v_pk_mul_f32 v[42:43], v[42:43], v[152:153]
	v_pk_mul_f32 v[38:39], v[38:39], v[156:157]
	v_pk_mul_f32 v[48:49], v[48:49], v[150:151]
	v_pk_mul_f32 v[44:45], v[44:45], v[154:155]
	v_pk_mul_f32 v[40:41], v[40:41], v[158:159]
	v_pk_mul_f32 v[36:37], v[36:37], v[162:163]
	v_pk_mul_f32 v[34:35], v[34:35], v[160:161]
	v_pk_mul_f32 v[30:31], v[30:31], v[148:149]
	v_pk_mul_f32 v[26:27], v[26:27], v[152:153]
	v_pk_mul_f32 v[22:23], v[22:23], v[156:157]
	v_pk_mul_f32 v[32:33], v[32:33], v[150:151]
	v_pk_mul_f32 v[28:29], v[28:29], v[154:155]
	v_pk_mul_f32 v[24:25], v[24:25], v[158:159]
	v_pk_mul_f32 v[20:21], v[20:21], v[162:163]
	v_pk_mul_f32 v[18:19], v[18:19], v[160:161]
	s_branch .LBB0_1354

.LBB0_1354:
	v_cndmask_b32_e64 v211, v169, v173, s[18:19]
	v_mul_f32_e32 v148, 0xbdd53b94, v211
	v_mov_b32_e32 v149, v148
	v_fmamk_f32 v82, v82, 0x3dd53b94, v148
	v_fmamk_f32 v83, v83, 0x3dd53b94, v148
	v_fmamk_f32 v84, v84, 0x3dd53b94, v148
	v_fmamk_f32 v85, v85, 0x3dd53b94, v148
	v_fmamk_f32 v86, v86, 0x3dd53b94, v148
	v_fmamk_f32 v87, v87, 0x3dd53b94, v148
	v_fmamk_f32 v88, v88, 0x3dd53b94, v148
	v_fmamk_f32 v89, v89, 0x3dd53b94, v148
	v_fmamk_f32 v90, v90, 0x3dd53b94, v148
	v_fmamk_f32 v91, v91, 0x3dd53b94, v148
	v_fmamk_f32 v92, v92, 0x3dd53b94, v148
	v_fmamk_f32 v93, v93, 0x3dd53b94, v148
	v_fmamk_f32 v94, v94, 0x3dd53b94, v148
	v_fmamk_f32 v95, v95, 0x3dd53b94, v148
	v_fmamk_f32 v96, v96, 0x3dd53b94, v148
	v_fmac_f32_e32 v149, 0x3dd53b94, v97
	v_exp_f32_e32 v169, v82
	v_exp_f32_e32 v191, v83
	v_exp_f32_e32 v170, v84
	v_exp_f32_e32 v192, v85
	v_exp_f32_e32 v190, v86
	v_exp_f32_e32 v193, v87
	v_exp_f32_e32 v171, v88
	v_exp_f32_e32 v189, v89
	v_exp_f32_e32 v173, v90
	v_exp_f32_e32 v175, v91
	v_exp_f32_e32 v174, v92
	v_exp_f32_e32 v188, v93
	v_exp_f32_e32 v164, v94
	v_exp_f32_e32 v166, v95
	v_exp_f32_e32 v165, v96
	v_exp_f32_e32 v167, v149
	v_pk_fma_f32 v[162:163], v[66:67], s[56:57], v[148:149] op_sel_hi:[1,0,0]
	v_add_f32_e32 v66, v212, v213
	v_fmac_f32_e32 v66, v210, v199
	v_add_f32_e32 v199, v229, v230
	s_add_i32 s8, s8, 2
	v_pk_fma_f32 v[160:161], v[68:69], s[56:57], v[148:149] op_sel_hi:[1,0,0]
	v_pk_fma_f32 v[156:157], v[70:71], s[56:57], v[148:149] op_sel_hi:[1,0,0]
	v_pk_fma_f32 v[152:153], v[72:73], s[56:57], v[148:149] op_sel_hi:[1,0,0]
	v_pk_fma_f32 v[150:151], v[74:75], s[56:57], v[148:149] op_sel_hi:[1,0,0]
	v_pk_fma_f32 v[158:159], v[76:77], s[56:57], v[148:149] op_sel_hi:[1,0,0]
	v_pk_fma_f32 v[154:155], v[78:79], s[56:57], v[148:149] op_sel_hi:[1,0,0]
	v_pk_fma_f32 v[148:149], v[80:81], s[56:57], v[148:149] op_sel_hi:[1,0,0]
	v_fmac_f32_e32 v199, v66, v172
	s_waitcnt lgkmcnt(0)
	s_cmp_lg_u32 s98, 0
	s_cbranch_scc1 .Latt_p3b
	s_waitcnt vmcnt(0)
	s_barrier
